# speedup vs baseline: 1.0342x; 1.0147x over previous
_Z12scan2_kernelPKDF16_S0_S0_S0_S0_PKfS2_S2_S2_PDF16_PfS4_:
	s_and_b32 s3, s2, 7
	s_lshr_b32 s2, s2, 3
	s_lshl_b32 s3, s3, 5
	s_or_b32 s2, s2, s3
	s_load_dwordx8 s[4:11], s[0:1], 0x0
	s_load_dwordx8 s[12:19], s[0:1], 0x20
	s_load_dwordx4 s[20:23], s[0:1], 0x40
	s_load_dwordx2 s[24:25], s[0:1], 0x50
	s_and_b32 s26, s2, 3
	s_bfe_u32 s27, s2, 0x50002
	s_lshr_b32 s28, s2, 7
	s_lshl_b32 s29, s26, 3
	v_lshrrev_b32_e32 v1, 6, v0
	v_and_b32_e32 v2, 15, v0
	v_bfe_u32 v3, v0, 4, 2
	v_and_b32_e32 v42, 63, v0
	v_readfirstlane_b32 s40, v1
	v_mov_b32_e32 v43, v0
	v_lshrrev_b32_e32 v14, 4, v43
	v_and_b32_e32 v15, 15, v43
	v_and_b32_e32 v188, 15, v14
	v_xor_b32_e32 v15, v15, v188
	v_lshlrev_b32_e32 v15, 4, v15
	v_lshl_or_b32 v4, v14, 13, v15
	v_lshl_or_b32 v6, v14, 8, v15
	v_lshrrev_b32_e32 v14, 3, v43
	v_and_b32_e32 v15, 7, v43
	v_and_b32_e32 v188, 7, v14
	v_xor_b32_e32 v15, v15, v188
	v_lshlrev_b32_e32 v15, 4, v15
	v_lshl_or_b32 v8, v14, 12, v15
	v_lshlrev_b32_e32 v40, 4, v43
	v_add_u32_e32 v32, 0xc800, v40
	v_add_u32_e32 v43, 0x200, v0
	v_lshrrev_b32_e32 v14, 4, v43
	v_and_b32_e32 v15, 15, v43
	v_and_b32_e32 v188, 15, v14
	v_xor_b32_e32 v15, v15, v188
	v_lshlrev_b32_e32 v15, 4, v15
	v_lshl_or_b32 v5, v14, 13, v15
	v_lshl_or_b32 v7, v14, 8, v15
	v_lshrrev_b32_e32 v14, 3, v43
	v_and_b32_e32 v15, 7, v43
	v_and_b32_e32 v188, 7, v14
	v_xor_b32_e32 v15, v15, v188
	v_lshlrev_b32_e32 v15, 4, v15
	v_lshl_or_b32 v9, v14, 12, v15
	v_lshlrev_b32_e32 v41, 4, v43
	v_add_u32_e32 v33, 0xc800, v41
	s_sub_u32 s45, 11, s40
	s_cmp_lt_u32 s40, 4
	s_cselect_b32 s41, s40, s45
	s_lshr_b32 s42, s41, 1
	s_lshl_b32 s43, s40, 10
	s_lshl_b32 s44, s40, 8
	s_and_b32 s45, s40, 1
	s_lshl_b32 s45, s45, 8
	v_lshl_add_u32 v10, v42, 2, s45
	s_lshl_b32 s45, s41, 4
	v_add_u32_e32 v14, s45, v2
	v_add_u32_e32 v15, 0, v3
	v_xor_b32_e32 v15, v15, v2
	v_lshlrev_b32_e32 v15, 4, v15
	v_lshl_or_b32 v16, v2, 8, v15
	v_add_u32_e32 v20, 0xc800, v16
	v_add_u32_e32 v15, 4, v3
	v_xor_b32_e32 v15, v15, v2
	v_lshlrev_b32_e32 v15, 4, v15
	v_lshl_or_b32 v17, v2, 8, v15
	v_add_u32_e32 v21, 0xc800, v17
	v_add_u32_e32 v15, 8, v3
	v_xor_b32_e32 v15, v15, v2
	v_lshlrev_b32_e32 v15, 4, v15
	v_lshl_or_b32 v18, v2, 8, v15
	v_add_u32_e32 v22, 0xc800, v18
	v_add_u32_e32 v15, 12, v3
	v_xor_b32_e32 v15, v15, v2
	v_lshlrev_b32_e32 v15, 4, v15
	v_lshl_or_b32 v19, v2, 8, v15
	v_add_u32_e32 v23, 0xc800, v19
	v_lshrrev_b32_e32 v188, 1, v3
	v_and_b32_e32 v189, 7, v14
	v_and_b32_e32 v190, 1, v3
	v_lshlrev_b32_e32 v190, 3, v190
	v_lshl_or_b32 v190, v14, 7, v190
	v_add_u32_e32 v15, 0, v188
	v_xor_b32_e32 v15, v15, v189
	v_lshl_add_u32 v24, v15, 4, v190
	v_add_u32_e32 v28, 0xc800, v24
	v_add_u32_e32 v15, 2, v188
	v_xor_b32_e32 v15, v15, v189
	v_lshl_add_u32 v25, v15, 4, v190
	v_add_u32_e32 v29, 0xc800, v25
	v_add_u32_e32 v15, 4, v188
	v_xor_b32_e32 v15, v15, v189
	v_lshl_add_u32 v26, v15, 4, v190
	v_add_u32_e32 v30, 0xc800, v26
	v_add_u32_e32 v15, 6, v188
	v_xor_b32_e32 v15, v15, v189
	v_lshl_add_u32 v27, v15, 4, v190
	v_add_u32_e32 v31, 0xc800, v27
	v_lshlrev_b32_e32 v242, 12, v14
	v_lshl_add_u32 v242, v3, 3, v242
	v_lshlrev_b32_e32 v36, 2, v14
	v_add_u32_e32 v37, 0xc800, v36
	v_lshlrev_b32_e32 v38, 5, v3
	v_add_u32_e32 v39, 0xc800, v38
	s_and_b32 s45, s41, 1
	s_lshl_b32 s45, s45, 4
	v_add_u32_e32 v43, s45, v2
	v_lshlrev_b32_e32 v189, 3, v3
	v_sub_u32_e32 v43, v43, v189
	v_cmp_le_i32_e64 s[52:53], 0, v43
	v_cmp_le_i32_e64 s[54:55], 1, v43
	v_cmp_le_i32_e64 s[56:57], 2, v43
	v_cmp_le_i32_e64 s[58:59], 3, v43
	v_cmp_le_i32_e64 s[60:61], 4, v43
	v_cmp_le_i32_e64 s[62:63], 5, v43
	v_cmp_le_i32_e64 s[64:65], 6, v43
	v_cmp_le_i32_e64 s[66:67], 7, v43
	v_cmp_eq_u32_e32 vcc, 0, v43
	s_nop 1
	v_cndmask_b32_e64 v188, 0, 1.0, vcc
	v_cmp_eq_u32_e32 vcc, 1, v43
	s_nop 1
	v_cndmask_b32_e64 v189, 0, 1.0, vcc
	v_cmp_eq_u32_e32 vcc, 2, v43
	s_nop 1
	v_cndmask_b32_e64 v190, 0, 1.0, vcc
	v_cmp_eq_u32_e32 vcc, 3, v43
	s_nop 1
	v_cndmask_b32_e64 v191, 0, 1.0, vcc
	v_cmp_eq_u32_e32 vcc, 4, v43
	s_nop 1
	v_cndmask_b32_e64 v192, 0, 1.0, vcc
	v_cmp_eq_u32_e32 vcc, 5, v43
	s_nop 1
	v_cndmask_b32_e64 v193, 0, 1.0, vcc
	v_cmp_eq_u32_e32 vcc, 6, v43
	s_nop 1
	v_cndmask_b32_e64 v194, 0, 1.0, vcc
	v_cmp_eq_u32_e32 vcc, 7, v43
	s_nop 1
	v_cndmask_b32_e64 v195, 0, 1.0, vcc
	v_cvt_pk_f16_f32 v92, v188, v189
	v_cvt_pk_f16_f32 v93, v190, v191
	v_cvt_pk_f16_f32 v94, v192, v193
	v_cvt_pk_f16_f32 v95, v194, v195
	v_mov_b32_e32 v250, 0
	v_mov_b32_e32 v251, 0
	s_waitcnt lgkmcnt(0)
	s_lshl_b32 s45, s28, 12
	s_lshl_b32 s48, s27, 7
	s_add_u32 s45, s45, s48
	s_lshl_b32 s48, s45, 9
	s_add_u32 s48, s4, s48
	s_addc_u32 s49, s5, 0
	v_lshlrev_b32_e32 v188, 9, v14
	v_lshl_add_u32 v188, v3, 4, v188
	global_load_dwordx4 v[44:47], v188, s[48:49] offset:256
	global_load_dwordx4 v[48:51], v188, s[48:49] offset:320
	global_load_dwordx4 v[52:55], v188, s[48:49] offset:384
	global_load_dwordx4 v[56:59], v188, s[48:49] offset:448
	s_lshl_b32 s48, s28, 5
	s_add_u32 s48, s48, s27
	s_lshl_b32 s48, s48, 15
	s_add_u32 s48, s10, s48
	s_addc_u32 s49, s11, 0
	v_lshlrev_b32_e32 v188, 8, v14
	v_lshl_add_u32 v188, v3, 4, v188
	global_load_dwordx4 v[144:147], v188, s[48:49] offset:0
	global_load_dwordx4 v[148:151], v188, s[48:49] offset:64
	global_load_dwordx4 v[152:155], v188, s[48:49] offset:128
	global_load_dwordx4 v[156:159], v188, s[48:49] offset:192
	v_and_b32_e32 v188, 7, v42
	v_add_u32_e32 v188, s29, v188
	v_lshlrev_b32_e32 v188, 2, v188
	global_load_dword v11, v188, s[20:21]
	global_load_dword v12, v188, s[18:19]
	s_mul_i32 s48, s28, 0x900
	s_lshl_b32 s49, s29, 6
	s_add_u32 s48, s48, s49
	s_lshl_b32 s48, s48, 13
	s_lshl_b32 s49, s27, 8
	s_add_u32 s48, s48, s49
	s_add_u32 s30, s6, s48
	s_addc_u32 s31, s7, 0
	s_lshl_b32 s48, s28, 5
	s_add_u32 s48, s48, s27
	s_lshl_b32 s48, s48, 5
	s_add_u32 s48, s48, s29
	s_lshl_b32 s48, s48, 14
	s_add_u32 s32, s12, s48
	s_addc_u32 s33, s13, 0
	s_lshl_b32 s48, s45, 12
	s_lshl_b32 s49, s29, 7
	s_add_u32 s48, s48, s49
	s_add_u32 s34, s8, s48
	s_addc_u32 s35, s9, 0
	s_add_u32 s38, s22, s48
	s_addc_u32 s39, s23, 0
	s_lshl_b32 s48, s28, 5
	s_add_u32 s48, s48, s29
	s_lshl_b32 s48, s48, 14
	s_lshl_b32 s49, s27, 9
	s_add_u32 s48, s48, s49
	s_lshr_b32 s49, s40, 1
	s_cmp_eq_u32 s49, 1
	s_cselect_b32 s50, s14, s16
	s_cselect_b32 s51, s15, s17
	s_add_u32 s36, s50, s48
	s_addc_u32 s37, s51, 0
	s_lshl_b32 s48, s45, 2
	s_add_u32 s24, s24, s48
	s_addc_u32 s25, s25, 0
	v_lshlrev_b32_e32 v15, 2, v14
	s_mov_b32 s51, 0xbfb8aa3b
	s_mov_b32 s50, 0x41800000
	s_add_u32 m0, s43, 0x0
	s_nop 0
	global_load_lds_dwordx4 v4, s[30:31]
	s_add_u32 m0, s43, 0x4000
	s_nop 0
	global_load_lds_dwordx4 v6, s[32:33]
	s_add_u32 m0, s43, 0x8000
	s_nop 0
	global_load_lds_dwordx4 v8, s[34:35]
	s_add_u32 m0, s43, 0x2000
	s_nop 0
	global_load_lds_dwordx4 v5, s[30:31]
	s_add_u32 m0, s43, 0x6000
	s_nop 0
	global_load_lds_dwordx4 v7, s[32:33]
	s_add_u32 m0, s43, 0xa000
	s_nop 0
	global_load_lds_dwordx4 v9, s[34:35]
	s_add_u32 m0, s44, 0xc000
	s_nop 0
	global_load_lds_dword v10, s[36:37]
	s_add_u32 s30, s30, 0x80000
	s_addc_u32 s31, s31, 0
	s_add_u32 s32, s32, 0x4000
	s_addc_u32 s33, s33, 0
	s_add_u32 s34, s34, 0x80
	s_addc_u32 s35, s35, 0
	s_add_u32 s36, s36, 0x4000
	s_addc_u32 s37, s37, 0
	global_load_dword v243, v10, s[36:37]
	global_load_dword v243, v10, s[36:37]
	global_load_dword v243, v10, s[36:37]
	global_load_dword v243, v10, s[36:37]
	s_waitcnt vmcnt(16)
	v_cvt_f32_f16_e32 v60, v144
	v_cvt_f32_f16_sdwa v61, v144 dst_sel:DWORD dst_unused:UNUSED_PAD src0_sel:WORD_1
	v_cvt_f32_f16_e32 v62, v145
	v_cvt_f32_f16_sdwa v63, v145 dst_sel:DWORD dst_unused:UNUSED_PAD src0_sel:WORD_1
	v_cvt_f32_f16_e32 v64, v146
	v_cvt_f32_f16_sdwa v65, v146 dst_sel:DWORD dst_unused:UNUSED_PAD src0_sel:WORD_1
	v_cvt_f32_f16_e32 v66, v147
	v_cvt_f32_f16_sdwa v67, v147 dst_sel:DWORD dst_unused:UNUSED_PAD src0_sel:WORD_1
	s_waitcnt vmcnt(15)
	v_cvt_f32_f16_e32 v68, v148
	v_cvt_f32_f16_sdwa v69, v148 dst_sel:DWORD dst_unused:UNUSED_PAD src0_sel:WORD_1
	v_cvt_f32_f16_e32 v70, v149
	v_cvt_f32_f16_sdwa v71, v149 dst_sel:DWORD dst_unused:UNUSED_PAD src0_sel:WORD_1
	v_cvt_f32_f16_e32 v72, v150
	v_cvt_f32_f16_sdwa v73, v150 dst_sel:DWORD dst_unused:UNUSED_PAD src0_sel:WORD_1
	v_cvt_f32_f16_e32 v74, v151
	v_cvt_f32_f16_sdwa v75, v151 dst_sel:DWORD dst_unused:UNUSED_PAD src0_sel:WORD_1
	s_waitcnt vmcnt(14)
	v_cvt_f32_f16_e32 v76, v152
	v_cvt_f32_f16_sdwa v77, v152 dst_sel:DWORD dst_unused:UNUSED_PAD src0_sel:WORD_1
	v_cvt_f32_f16_e32 v78, v153
	v_cvt_f32_f16_sdwa v79, v153 dst_sel:DWORD dst_unused:UNUSED_PAD src0_sel:WORD_1
	v_cvt_f32_f16_e32 v80, v154
	v_cvt_f32_f16_sdwa v81, v154 dst_sel:DWORD dst_unused:UNUSED_PAD src0_sel:WORD_1
	v_cvt_f32_f16_e32 v82, v155
	v_cvt_f32_f16_sdwa v83, v155 dst_sel:DWORD dst_unused:UNUSED_PAD src0_sel:WORD_1
	s_waitcnt vmcnt(13)
	v_cvt_f32_f16_e32 v84, v156
	v_cvt_f32_f16_sdwa v85, v156 dst_sel:DWORD dst_unused:UNUSED_PAD src0_sel:WORD_1
	v_cvt_f32_f16_e32 v86, v157
	v_cvt_f32_f16_sdwa v87, v157 dst_sel:DWORD dst_unused:UNUSED_PAD src0_sel:WORD_1
	v_cvt_f32_f16_e32 v88, v158
	v_cvt_f32_f16_sdwa v89, v158 dst_sel:DWORD dst_unused:UNUSED_PAD src0_sel:WORD_1
	v_cvt_f32_f16_e32 v90, v159
	v_cvt_f32_f16_sdwa v91, v159 dst_sel:DWORD dst_unused:UNUSED_PAD src0_sel:WORD_1
	s_waitcnt vmcnt(11)
	s_waitcnt vmcnt(12)
	v_mul_f32_e32 v11, 0x41800000, v11
	s_mov_b32 s48, 0
.Lmy_s2_heads1:
	s_waitcnt vmcnt(4)
	s_add_u32 s49, s48, 0
	s_waitcnt lgkmcnt(0)
	s_barrier
	ds_read_b128 v[144:147], v16 offset:16384
	ds_read_b128 v[148:151], v16 offset:20480
	ds_read_b128 v[152:155], v16 offset:24576
	ds_read_b128 v[156:159], v16 offset:28672
	ds_read_b32 v189, v36 offset:49152
	s_cmp_lt_u32 s49, 7
	s_cbranch_scc0 .Lmy_s2_nodma2
	s_add_u32 m0, s43, 0xc800
	s_nop 0
	global_load_lds_dwordx4 v4, s[30:31]
	s_add_u32 m0, s43, 0x10800
	s_nop 0
	global_load_lds_dwordx4 v6, s[32:33]
	s_add_u32 m0, s43, 0x14800
	s_nop 0
	global_load_lds_dwordx4 v8, s[34:35]
	s_add_u32 m0, s43, 0xe800
	s_nop 0
	global_load_lds_dwordx4 v5, s[30:31]
	s_add_u32 m0, s43, 0x12800
	s_nop 0
	global_load_lds_dwordx4 v7, s[32:33]
	s_add_u32 m0, s43, 0x16800
	s_nop 0
	global_load_lds_dwordx4 v9, s[34:35]
	s_add_u32 m0, s44, 0x18800
	s_nop 0
	global_load_lds_dword v10, s[36:37]
	s_add_u32 s30, s30, 0x80000
	s_addc_u32 s31, s31, 0
	s_add_u32 s32, s32, 0x4000
	s_addc_u32 s33, s33, 0
	s_add_u32 s34, s34, 0x80
	s_addc_u32 s35, s35, 0
	s_add_u32 s36, s36, 0x4000
	s_addc_u32 s37, s37, 0
.Lmy_s2_nodma2:
	ds_read_b128 v[160:163], v17 offset:16384
	ds_read_b128 v[164:167], v17 offset:20480
	ds_read_b128 v[168:171], v17 offset:24576
	ds_read_b128 v[172:175], v17 offset:28672
	s_waitcnt lgkmcnt(4)
	v_mfma_f32_16x16x32_f16 v[96:99], v[144:147], v[44:47], 0
	v_mfma_f32_16x16x32_f16 v[100:103], v[148:151], v[44:47], 0
	v_mfma_f32_16x16x32_f16 v[104:107], v[152:155], v[44:47], 0
	v_mfma_f32_16x16x32_f16 v[108:111], v[156:159], v[44:47], 0
	ds_read_b128 v[144:147], v18 offset:16384
	ds_read_b128 v[148:151], v18 offset:20480
	ds_read_b128 v[152:155], v18 offset:24576
	ds_read_b128 v[156:159], v18 offset:28672
	s_waitcnt lgkmcnt(4)
	v_mfma_f32_16x16x32_f16 v[96:99], v[160:163], v[48:51], v[96:99]
	v_mfma_f32_16x16x32_f16 v[100:103], v[164:167], v[48:51], v[100:103]
	v_mfma_f32_16x16x32_f16 v[104:107], v[168:171], v[48:51], v[104:107]
	v_mfma_f32_16x16x32_f16 v[108:111], v[172:175], v[48:51], v[108:111]
	ds_read_b128 v[160:163], v19 offset:16384
	ds_read_b128 v[164:167], v19 offset:20480
	ds_read_b128 v[168:171], v19 offset:24576
	ds_read_b128 v[172:175], v19 offset:28672
	s_waitcnt lgkmcnt(4)
	v_mfma_f32_16x16x32_f16 v[96:99], v[144:147], v[52:55], v[96:99]
	v_mfma_f32_16x16x32_f16 v[100:103], v[148:151], v[52:55], v[100:103]
	v_mfma_f32_16x16x32_f16 v[104:107], v[152:155], v[52:55], v[104:107]
	v_mfma_f32_16x16x32_f16 v[108:111], v[156:159], v[52:55], v[108:111]
	ds_read_b128 v[176:179], v38 offset:49664
	ds_read_b128 v[180:183], v38 offset:49680
	ds_read_b32 v188, v38 offset:49152
	ds_read_b128 v[144:147], v16 offset:0
	ds_read_b128 v[148:151], v16 offset:4096
	ds_read_b128 v[152:155], v16 offset:8192
	ds_read_b128 v[156:159], v16 offset:12288
	s_waitcnt lgkmcnt(7)
	v_mfma_f32_16x16x32_f16 v[96:99], v[160:163], v[56:59], v[96:99]
	v_mfma_f32_16x16x32_f16 v[100:103], v[164:167], v[56:59], v[100:103]
	v_mfma_f32_16x16x32_f16 v[104:107], v[168:171], v[56:59], v[104:107]
	v_mfma_f32_16x16x32_f16 v[108:111], v[172:175], v[56:59], v[108:111]
	v_mul_f32_e32 v189, 0x3fb8aa3b, v189
	s_cmp_lt_u32 s42, 0
	s_cbranch_scc1 .Lmy_s2_kend3
	s_cmp_eq_u32 s42, 0
	s_cbranch_scc1 .Lmy_s2_diag4
	ds_read_b128 v[224:227], v38 offset:49792
	ds_read_b128 v[228:231], v38 offset:49808
	ds_read_b32 v232, v38 offset:49280
	ds_read_b128 v[160:163], v17 offset:0
	ds_read_b128 v[164:167], v17 offset:4096
	ds_read_b128 v[168:171], v17 offset:8192
	ds_read_b128 v[172:175], v17 offset:12288
	s_waitcnt lgkmcnt(7)
	v_fma_f32 v188, v188, s51, v189
	v_exp_f32_e32 v188, v188
	s_nop 0
	v_pk_mul_f32 v[176:177], v[176:177], v[188:189] op_sel_hi:[1,0]
	v_pk_mul_f32 v[178:179], v[178:179], v[188:189] op_sel_hi:[1,0]
	v_pk_mul_f32 v[180:181], v[180:181], v[188:189] op_sel_hi:[1,0]
	v_pk_mul_f32 v[182:183], v[182:183], v[188:189] op_sel_hi:[1,0]
	v_pk_mul_f32 v[176:177], v[60:61], v[176:177]
	v_pk_mul_f32 v[178:179], v[62:63], v[178:179]
	v_pk_mul_f32 v[180:181], v[64:65], v[180:181]
	v_pk_mul_f32 v[182:183], v[66:67], v[182:183]
	v_cvt_pk_f16_f32 v184, v176, v177
	v_cvt_pk_f16_f32 v185, v178, v179
	v_cvt_pk_f16_f32 v186, v180, v181
	v_cvt_pk_f16_f32 v187, v182, v183
	s_nop 1
	v_mfma_f32_16x16x32_f16 v[112:115], v[144:147], v[184:187], 0
	v_mfma_f32_16x16x32_f16 v[116:119], v[148:151], v[184:187], 0
	v_mfma_f32_16x16x32_f16 v[120:123], v[152:155], v[184:187], 0
	v_mfma_f32_16x16x32_f16 v[124:127], v[156:159], v[184:187], 0
	s_branch .Lmy_s2_knext5

.Lmy_s2_knext11:
.Lmy_s2_kend3:
	v_readlane_b32 s46, v11, s49
	v_readlane_b32 s47, v12, s49
	v_exp_f32_e32 v190, v189
	s_waitcnt lgkmcnt(0)
	s_nop 7
	v_cvt_f32_f16_e32 v198, v234
	v_cvt_f32_f16_sdwa v199, v234 dst_sel:DWORD dst_unused:UNUSED_PAD src0_sel:WORD_1
	v_cvt_f32_f16_e32 v200, v235
	v_cvt_f32_f16_sdwa v201, v235 dst_sel:DWORD dst_unused:UNUSED_PAD src0_sel:WORD_1
	v_pk_fma_f32 v[192:193], v[190:191], v[96:97], v[112:113] op_sel_hi:[0,1,1]
	v_pk_fma_f32 v[194:195], v[190:191], v[98:99], v[114:115] op_sel_hi:[0,1,1]
	v_pk_mul_f32 v[192:193], v[192:193], s[46:47] op_sel:[0,1] op_sel_hi:[1,1]
	v_pk_mul_f32 v[194:195], v[194:195], s[46:47] op_sel:[0,1] op_sel_hi:[1,1]
	v_pk_fma_f32 v[192:193], s[46:47], v[128:129], v[192:193] op_sel_hi:[0,1,1]
	v_pk_fma_f32 v[194:195], s[46:47], v[130:131], v[194:195] op_sel_hi:[0,1,1]
	v_pk_mul_f32 v[192:193], v[192:193], v[198:199]
	v_pk_mul_f32 v[194:195], v[194:195], v[200:201]
	v_pk_fma_f32 v[250:251], v[192:193], v[192:193], v[250:251]
	v_pk_fma_f32 v[250:251], v[194:195], v[194:195], v[250:251]
	v_cvt_pk_f16_f32 v196, v192, v193
	v_cvt_pk_f16_f32 v197, v194, v195
	global_store_dwordx2 v242, v[196:197], s[38:39]
	v_cvt_f32_f16_e32 v198, v236
	v_cvt_f32_f16_sdwa v199, v236 dst_sel:DWORD dst_unused:UNUSED_PAD src0_sel:WORD_1
	v_cvt_f32_f16_e32 v200, v237
	v_cvt_f32_f16_sdwa v201, v237 dst_sel:DWORD dst_unused:UNUSED_PAD src0_sel:WORD_1
	v_pk_fma_f32 v[192:193], v[190:191], v[100:101], v[116:117] op_sel_hi:[0,1,1]
	v_pk_fma_f32 v[194:195], v[190:191], v[102:103], v[118:119] op_sel_hi:[0,1,1]
	v_pk_mul_f32 v[192:193], v[192:193], s[46:47] op_sel:[0,1] op_sel_hi:[1,1]
	v_pk_mul_f32 v[194:195], v[194:195], s[46:47] op_sel:[0,1] op_sel_hi:[1,1]
	v_pk_fma_f32 v[192:193], s[46:47], v[132:133], v[192:193] op_sel_hi:[0,1,1]
	v_pk_fma_f32 v[194:195], s[46:47], v[134:135], v[194:195] op_sel_hi:[0,1,1]
	v_pk_mul_f32 v[192:193], v[192:193], v[198:199]
	v_pk_mul_f32 v[194:195], v[194:195], v[200:201]
	v_pk_fma_f32 v[250:251], v[192:193], v[192:193], v[250:251]
	v_pk_fma_f32 v[250:251], v[194:195], v[194:195], v[250:251]
	v_cvt_pk_f16_f32 v196, v192, v193
	v_cvt_pk_f16_f32 v197, v194, v195
	global_store_dwordx2 v242, v[196:197], s[38:39] offset:32
	v_cvt_f32_f16_e32 v198, v238
	v_cvt_f32_f16_sdwa v199, v238 dst_sel:DWORD dst_unused:UNUSED_PAD src0_sel:WORD_1
	v_cvt_f32_f16_e32 v200, v239
	v_cvt_f32_f16_sdwa v201, v239 dst_sel:DWORD dst_unused:UNUSED_PAD src0_sel:WORD_1
	v_pk_fma_f32 v[192:193], v[190:191], v[104:105], v[120:121] op_sel_hi:[0,1,1]
	v_pk_fma_f32 v[194:195], v[190:191], v[106:107], v[122:123] op_sel_hi:[0,1,1]
	v_pk_mul_f32 v[192:193], v[192:193], s[46:47] op_sel:[0,1] op_sel_hi:[1,1]
	v_pk_mul_f32 v[194:195], v[194:195], s[46:47] op_sel:[0,1] op_sel_hi:[1,1]
	v_pk_fma_f32 v[192:193], s[46:47], v[136:137], v[192:193] op_sel_hi:[0,1,1]
	v_pk_fma_f32 v[194:195], s[46:47], v[138:139], v[194:195] op_sel_hi:[0,1,1]
	v_pk_mul_f32 v[192:193], v[192:193], v[198:199]
	v_pk_mul_f32 v[194:195], v[194:195], v[200:201]
	v_pk_fma_f32 v[250:251], v[192:193], v[192:193], v[250:251]
	v_pk_fma_f32 v[250:251], v[194:195], v[194:195], v[250:251]
	v_cvt_pk_f16_f32 v196, v192, v193
	v_cvt_pk_f16_f32 v197, v194, v195
	global_store_dwordx2 v242, v[196:197], s[38:39] offset:64
	v_cvt_f32_f16_e32 v198, v240
	v_cvt_f32_f16_sdwa v199, v240 dst_sel:DWORD dst_unused:UNUSED_PAD src0_sel:WORD_1
	v_cvt_f32_f16_e32 v200, v241
	v_cvt_f32_f16_sdwa v201, v241 dst_sel:DWORD dst_unused:UNUSED_PAD src0_sel:WORD_1
	v_pk_fma_f32 v[192:193], v[190:191], v[108:109], v[124:125] op_sel_hi:[0,1,1]
	v_pk_fma_f32 v[194:195], v[190:191], v[110:111], v[126:127] op_sel_hi:[0,1,1]
	v_pk_mul_f32 v[192:193], v[192:193], s[46:47] op_sel:[0,1] op_sel_hi:[1,1]
	v_pk_mul_f32 v[194:195], v[194:195], s[46:47] op_sel:[0,1] op_sel_hi:[1,1]
	v_pk_fma_f32 v[192:193], s[46:47], v[140:141], v[192:193] op_sel_hi:[0,1,1]
	v_pk_fma_f32 v[194:195], s[46:47], v[142:143], v[194:195] op_sel_hi:[0,1,1]
	v_pk_mul_f32 v[192:193], v[192:193], v[198:199]
	v_pk_mul_f32 v[194:195], v[194:195], v[200:201]
	v_pk_fma_f32 v[250:251], v[192:193], v[192:193], v[250:251]
	v_pk_fma_f32 v[250:251], v[194:195], v[194:195], v[250:251]
	v_cvt_pk_f16_f32 v196, v192, v193
	v_cvt_pk_f16_f32 v197, v194, v195
	global_store_dwordx2 v242, v[196:197], s[38:39] offset:96
	s_add_u32 s38, s38, 0x80
	s_addc_u32 s39, s39, 0
	s_waitcnt vmcnt(4)
	s_add_u32 s49, s48, 1
	s_waitcnt lgkmcnt(0)
	s_barrier
	ds_read_b128 v[144:147], v20 offset:16384
	ds_read_b128 v[148:151], v20 offset:20480
	ds_read_b128 v[152:155], v20 offset:24576
	ds_read_b128 v[156:159], v20 offset:28672
	ds_read_b32 v189, v37 offset:49152
	s_cmp_lt_u32 s49, 7
	s_cbranch_scc0 .Lmy_s2_nodma12
	s_add_u32 m0, s43, 0x0
	s_nop 0
	global_load_lds_dwordx4 v4, s[30:31]
	s_add_u32 m0, s43, 0x4000
	s_nop 0
	global_load_lds_dwordx4 v6, s[32:33]
	s_add_u32 m0, s43, 0x8000
	s_nop 0
	global_load_lds_dwordx4 v8, s[34:35]
	s_add_u32 m0, s43, 0x2000
	s_nop 0
	global_load_lds_dwordx4 v5, s[30:31]
	s_add_u32 m0, s43, 0x6000
	s_nop 0
	global_load_lds_dwordx4 v7, s[32:33]
	s_add_u32 m0, s43, 0xa000
	s_nop 0
	global_load_lds_dwordx4 v9, s[34:35]
	s_add_u32 m0, s44, 0xc000
	s_nop 0
	global_load_lds_dword v10, s[36:37]
	s_add_u32 s30, s30, 0x80000
	s_addc_u32 s31, s31, 0
	s_add_u32 s32, s32, 0x4000
	s_addc_u32 s33, s33, 0
	s_add_u32 s34, s34, 0x80
	s_addc_u32 s35, s35, 0
	s_add_u32 s36, s36, 0x4000
	s_addc_u32 s37, s37, 0
.Lmy_s2_nodma12:
	ds_read_b128 v[160:163], v21 offset:16384
	ds_read_b128 v[164:167], v21 offset:20480
	ds_read_b128 v[168:171], v21 offset:24576
	ds_read_b128 v[172:175], v21 offset:28672
	s_waitcnt lgkmcnt(4)
	v_mfma_f32_16x16x32_f16 v[96:99], v[144:147], v[44:47], 0
	v_mfma_f32_16x16x32_f16 v[100:103], v[148:151], v[44:47], 0
	v_mfma_f32_16x16x32_f16 v[104:107], v[152:155], v[44:47], 0
	v_mfma_f32_16x16x32_f16 v[108:111], v[156:159], v[44:47], 0
	ds_read_b128 v[144:147], v22 offset:16384
	ds_read_b128 v[148:151], v22 offset:20480
	ds_read_b128 v[152:155], v22 offset:24576
	ds_read_b128 v[156:159], v22 offset:28672
	s_waitcnt lgkmcnt(4)
	v_mfma_f32_16x16x32_f16 v[96:99], v[160:163], v[48:51], v[96:99]
	v_mfma_f32_16x16x32_f16 v[100:103], v[164:167], v[48:51], v[100:103]
	v_mfma_f32_16x16x32_f16 v[104:107], v[168:171], v[48:51], v[104:107]
	v_mfma_f32_16x16x32_f16 v[108:111], v[172:175], v[48:51], v[108:111]
	ds_read_b128 v[160:163], v23 offset:16384
	ds_read_b128 v[164:167], v23 offset:20480
	ds_read_b128 v[168:171], v23 offset:24576
	ds_read_b128 v[172:175], v23 offset:28672
	s_waitcnt lgkmcnt(4)
	v_mfma_f32_16x16x32_f16 v[96:99], v[144:147], v[52:55], v[96:99]
	v_mfma_f32_16x16x32_f16 v[100:103], v[148:151], v[52:55], v[100:103]
	v_mfma_f32_16x16x32_f16 v[104:107], v[152:155], v[52:55], v[104:107]
	v_mfma_f32_16x16x32_f16 v[108:111], v[156:159], v[52:55], v[108:111]
	ds_read_b128 v[176:179], v39 offset:49664
	ds_read_b128 v[180:183], v39 offset:49680
	ds_read_b32 v188, v39 offset:49152
	ds_read_b128 v[144:147], v20 offset:0
	ds_read_b128 v[148:151], v20 offset:4096
	ds_read_b128 v[152:155], v20 offset:8192
	ds_read_b128 v[156:159], v20 offset:12288
	s_waitcnt lgkmcnt(7)
	v_mfma_f32_16x16x32_f16 v[96:99], v[160:163], v[56:59], v[96:99]
	v_mfma_f32_16x16x32_f16 v[100:103], v[164:167], v[56:59], v[100:103]
	v_mfma_f32_16x16x32_f16 v[104:107], v[168:171], v[56:59], v[104:107]
	v_mfma_f32_16x16x32_f16 v[108:111], v[172:175], v[56:59], v[108:111]
	v_mul_f32_e32 v189, 0x3fb8aa3b, v189
	s_cmp_lt_u32 s42, 0
	s_cbranch_scc1 .Lmy_s2_kend13
	s_cmp_eq_u32 s42, 0
	s_cbranch_scc1 .Lmy_s2_diag14
	ds_read_b128 v[224:227], v39 offset:49792
	ds_read_b128 v[228:231], v39 offset:49808
	ds_read_b32 v232, v39 offset:49280
	ds_read_b128 v[160:163], v21 offset:0
	ds_read_b128 v[164:167], v21 offset:4096
	ds_read_b128 v[168:171], v21 offset:8192
	ds_read_b128 v[172:175], v21 offset:12288
	s_waitcnt lgkmcnt(7)
	v_fma_f32 v188, v188, s51, v189
	v_exp_f32_e32 v188, v188
	s_nop 0
	v_pk_mul_f32 v[176:177], v[176:177], v[188:189] op_sel_hi:[1,0]
	v_pk_mul_f32 v[178:179], v[178:179], v[188:189] op_sel_hi:[1,0]
	v_pk_mul_f32 v[180:181], v[180:181], v[188:189] op_sel_hi:[1,0]
	v_pk_mul_f32 v[182:183], v[182:183], v[188:189] op_sel_hi:[1,0]
	v_pk_mul_f32 v[176:177], v[60:61], v[176:177]
	v_pk_mul_f32 v[178:179], v[62:63], v[178:179]
	v_pk_mul_f32 v[180:181], v[64:65], v[180:181]
	v_pk_mul_f32 v[182:183], v[66:67], v[182:183]
	v_cvt_pk_f16_f32 v184, v176, v177
	v_cvt_pk_f16_f32 v185, v178, v179
	v_cvt_pk_f16_f32 v186, v180, v181
	v_cvt_pk_f16_f32 v187, v182, v183
	s_nop 1
	v_mfma_f32_16x16x32_f16 v[112:115], v[144:147], v[184:187], 0
	v_mfma_f32_16x16x32_f16 v[116:119], v[148:151], v[184:187], 0
	v_mfma_f32_16x16x32_f16 v[120:123], v[152:155], v[184:187], 0
	v_mfma_f32_16x16x32_f16 v[124:127], v[156:159], v[184:187], 0
	s_branch .Lmy_s2_knext15

.Lmy_s2_knext21:
.Lmy_s2_kend13:
	v_readlane_b32 s46, v11, s49
	v_readlane_b32 s47, v12, s49
	v_exp_f32_e32 v190, v189
	s_waitcnt lgkmcnt(0)
	s_nop 7
	v_cvt_f32_f16_e32 v198, v234
	v_cvt_f32_f16_sdwa v199, v234 dst_sel:DWORD dst_unused:UNUSED_PAD src0_sel:WORD_1
	v_cvt_f32_f16_e32 v200, v235
	v_cvt_f32_f16_sdwa v201, v235 dst_sel:DWORD dst_unused:UNUSED_PAD src0_sel:WORD_1
	v_pk_fma_f32 v[192:193], v[190:191], v[96:97], v[112:113] op_sel_hi:[0,1,1]
	v_pk_fma_f32 v[194:195], v[190:191], v[98:99], v[114:115] op_sel_hi:[0,1,1]
	v_pk_mul_f32 v[192:193], v[192:193], s[46:47] op_sel:[0,1] op_sel_hi:[1,1]
	v_pk_mul_f32 v[194:195], v[194:195], s[46:47] op_sel:[0,1] op_sel_hi:[1,1]
	v_pk_fma_f32 v[192:193], s[46:47], v[128:129], v[192:193] op_sel_hi:[0,1,1]
	v_pk_fma_f32 v[194:195], s[46:47], v[130:131], v[194:195] op_sel_hi:[0,1,1]
	v_pk_mul_f32 v[192:193], v[192:193], v[198:199]
	v_pk_mul_f32 v[194:195], v[194:195], v[200:201]
	v_pk_fma_f32 v[250:251], v[192:193], v[192:193], v[250:251]
	v_pk_fma_f32 v[250:251], v[194:195], v[194:195], v[250:251]
	v_cvt_pk_f16_f32 v196, v192, v193
	v_cvt_pk_f16_f32 v197, v194, v195
	global_store_dwordx2 v242, v[196:197], s[38:39]
	v_cvt_f32_f16_e32 v198, v236
	v_cvt_f32_f16_sdwa v199, v236 dst_sel:DWORD dst_unused:UNUSED_PAD src0_sel:WORD_1
	v_cvt_f32_f16_e32 v200, v237
	v_cvt_f32_f16_sdwa v201, v237 dst_sel:DWORD dst_unused:UNUSED_PAD src0_sel:WORD_1
	v_pk_fma_f32 v[192:193], v[190:191], v[100:101], v[116:117] op_sel_hi:[0,1,1]
	v_pk_fma_f32 v[194:195], v[190:191], v[102:103], v[118:119] op_sel_hi:[0,1,1]
	v_pk_mul_f32 v[192:193], v[192:193], s[46:47] op_sel:[0,1] op_sel_hi:[1,1]
	v_pk_mul_f32 v[194:195], v[194:195], s[46:47] op_sel:[0,1] op_sel_hi:[1,1]
	v_pk_fma_f32 v[192:193], s[46:47], v[132:133], v[192:193] op_sel_hi:[0,1,1]
	v_pk_fma_f32 v[194:195], s[46:47], v[134:135], v[194:195] op_sel_hi:[0,1,1]
	v_pk_mul_f32 v[192:193], v[192:193], v[198:199]
	v_pk_mul_f32 v[194:195], v[194:195], v[200:201]
	v_pk_fma_f32 v[250:251], v[192:193], v[192:193], v[250:251]
	v_pk_fma_f32 v[250:251], v[194:195], v[194:195], v[250:251]
	v_cvt_pk_f16_f32 v196, v192, v193
	v_cvt_pk_f16_f32 v197, v194, v195
	global_store_dwordx2 v242, v[196:197], s[38:39] offset:32
	v_cvt_f32_f16_e32 v198, v238
	v_cvt_f32_f16_sdwa v199, v238 dst_sel:DWORD dst_unused:UNUSED_PAD src0_sel:WORD_1
	v_cvt_f32_f16_e32 v200, v239
	v_cvt_f32_f16_sdwa v201, v239 dst_sel:DWORD dst_unused:UNUSED_PAD src0_sel:WORD_1
	v_pk_fma_f32 v[192:193], v[190:191], v[104:105], v[120:121] op_sel_hi:[0,1,1]
	v_pk_fma_f32 v[194:195], v[190:191], v[106:107], v[122:123] op_sel_hi:[0,1,1]
	v_pk_mul_f32 v[192:193], v[192:193], s[46:47] op_sel:[0,1] op_sel_hi:[1,1]
	v_pk_mul_f32 v[194:195], v[194:195], s[46:47] op_sel:[0,1] op_sel_hi:[1,1]
	v_pk_fma_f32 v[192:193], s[46:47], v[136:137], v[192:193] op_sel_hi:[0,1,1]
	v_pk_fma_f32 v[194:195], s[46:47], v[138:139], v[194:195] op_sel_hi:[0,1,1]
	v_pk_mul_f32 v[192:193], v[192:193], v[198:199]
	v_pk_mul_f32 v[194:195], v[194:195], v[200:201]
	v_pk_fma_f32 v[250:251], v[192:193], v[192:193], v[250:251]
	v_pk_fma_f32 v[250:251], v[194:195], v[194:195], v[250:251]
	v_cvt_pk_f16_f32 v196, v192, v193
	v_cvt_pk_f16_f32 v197, v194, v195
	global_store_dwordx2 v242, v[196:197], s[38:39] offset:64
	v_cvt_f32_f16_e32 v198, v240
	v_cvt_f32_f16_sdwa v199, v240 dst_sel:DWORD dst_unused:UNUSED_PAD src0_sel:WORD_1
	v_cvt_f32_f16_e32 v200, v241
	v_cvt_f32_f16_sdwa v201, v241 dst_sel:DWORD dst_unused:UNUSED_PAD src0_sel:WORD_1
	v_pk_fma_f32 v[192:193], v[190:191], v[108:109], v[124:125] op_sel_hi:[0,1,1]
	v_pk_fma_f32 v[194:195], v[190:191], v[110:111], v[126:127] op_sel_hi:[0,1,1]
	v_pk_mul_f32 v[192:193], v[192:193], s[46:47] op_sel:[0,1] op_sel_hi:[1,1]
	v_pk_mul_f32 v[194:195], v[194:195], s[46:47] op_sel:[0,1] op_sel_hi:[1,1]
	v_pk_fma_f32 v[192:193], s[46:47], v[140:141], v[192:193] op_sel_hi:[0,1,1]
	v_pk_fma_f32 v[194:195], s[46:47], v[142:143], v[194:195] op_sel_hi:[0,1,1]
	v_pk_mul_f32 v[192:193], v[192:193], v[198:199]
	v_pk_mul_f32 v[194:195], v[194:195], v[200:201]
	v_pk_fma_f32 v[250:251], v[192:193], v[192:193], v[250:251]
	v_pk_fma_f32 v[250:251], v[194:195], v[194:195], v[250:251]
	v_cvt_pk_f16_f32 v196, v192, v193
	v_cvt_pk_f16_f32 v197, v194, v195
	global_store_dwordx2 v242, v[196:197], s[38:39] offset:96
	s_add_u32 s38, s38, 0x80
	s_addc_u32 s39, s39, 0
	s_add_u32 s48, s48, 2
	s_cmp_lt_u32 s48, 8
	s_cbranch_scc1 .Lmy_s2_heads1
	v_add_f32_e32 v13, v250, v251
	v_mul_f32_e32 v13, 0x3b800000, v13
	v_mbcnt_lo_u32_b32 v188, -1, 0
	v_mbcnt_hi_u32_b32 v188, -1, v188
	v_xor_b32_e32 v189, 16, v188
	v_lshlrev_b32_e32 v189, 2, v189
	ds_bpermute_b32 v190, v189, v13
	s_waitcnt lgkmcnt(0)
	v_add_f32_e32 v13, v13, v190
	v_xor_b32_e32 v189, 32, v188
	v_lshlrev_b32_e32 v189, 2, v189
	ds_bpermute_b32 v190, v189, v13
	s_waitcnt lgkmcnt(0)
	v_add_f32_e32 v13, v13, v190
	v_cmp_gt_u32_e32 vcc, 16, v188
	s_and_saveexec_b64 s[48:49], vcc
	s_cbranch_execz .Lmy_s2_noat22
	global_atomic_add_f32 v15, v13, s[24:25]
